# cv_stream waves at s_setprio 1 while streaming
# baseline (speedup 1.0000x reference)
.LBB0_477:
	s_cmp_lt_i32 s46, 6
	s_cselect_b64 s[4:5], -1, 0
	s_and_b64 s[4:5], s[4:5], s[6:7]
	s_andn2_b64 vcc, exec, s[4:5]
	s_cbranch_vccnz .LBB0_1653
	s_mov_b64 s[4:5], s[0:1]
	v_mov_b32_e32 v1, v0
	s_nop 0
	v_cmp_gt_i32_e32 vcc, 2, v1
	s_and_saveexec_b64 s[6:7], vcc
	v_lshl_add_u32 v2, v1, 2, 0
	v_add_u32_e32 v2, 0x23fc0, v2
	v_mov_b32_e32 v3, 0
	ds_write_b32 v2, v3
	s_or_b64 exec, exec, s[6:7]
	v_and_b32_e32 v194, 63, v1
	s_cmpk_lt_u32 s66, 0x180
	s_waitcnt vmcnt(0) lgkmcnt(0)
	s_barrier
	s_cbranch_scc1 .LBB0_518
	s_setprio 1
	s_lshl_b32 s8, s2, 1
	s_add_i32 s8, s8, s52
	s_add_i32 s6, s8, -6
	s_cmp_gt_i32 s6, 0x17fff
	s_cbranch_scc1 .LBB0_518
	s_mul_i32 s9, s52, 0x4100
	s_lshl_b32 s3, s48, 1
	s_add_i32 s9, s9, 0
	v_lshlrev_b32_e32 v2, 2, v194
	v_lshrrev_b32_e32 v1, 1, v1
	v_and_b32_e32 v2, 60, v2
	v_lshlrev_b32_e32 v5, 4, v194
	s_add_u32 s43, s44, 0x23d40000
	v_and_b32_e32 v1, 24, v1
	v_mul_u32_u24_e32 v3, 0x50, v2
	v_lshrrev_b32_e32 v4, 2, v194
	v_and_b32_e32 v198, 48, v5
	s_addc_u32 s49, s45, 0
	v_mov_b32_e32 v197, 0
	v_add3_u32 v3, s9, v1, v3
	v_add_u32_e32 v5, s9, v198
	v_mul_u32_u24_e32 v6, 0x50, v4
	v_lshlrev_b32_e32 v200, 11, v4
	s_add_u32 s53, s44, 0x3d40000
	v_lshlrev_b32_e32 v208, 2, v2
	s_mov_b32 s7, 0
	v_mov_b32_e32 v199, v197
	v_mov_b32_e32 v201, v197
	v_or_b32_e32 v202, 0x8000, v200
	v_mov_b32_e32 v203, v197
	v_or_b32_e32 v204, 0x10000, v200
	v_mov_b32_e32 v205, v197
	v_or_b32_e32 v206, 0x18000, v200
	v_mov_b32_e32 v207, v197
	s_mul_i32 s42, s48, 12
	s_addc_u32 s54, s45, 0
	s_add_i32 s55, s8, 0xfffefffa
	s_lshl_b32 s56, s6, 1
	s_mul_i32 s57, s48, 24
	s_lshl_b32 s58, s6, 6
	s_mul_i32 s59, s48, 0x300
	s_lshl_b32 s60, s48, 2
	s_mul_i32 s61, s48, 6
	s_lshl_b32 s62, s48, 3
	s_mul_i32 s63, s48, 10
	v_mov_b32_e32 v210, v208
	v_mov_b32_e32 v211, v197
	s_mov_b32 s64, 0xc3e00000
	v_mov_b32_e32 v195, 0x43e00000
	v_add_u32_e32 v212, v5, v6
	v_add_u32_e32 v213, 0x2000, v3
	s_branch .LBB0_484

.LBB0_518:
	s_setprio 0
	s_add_u32 s3, s44, 0x70098000
	s_addc_u32 s26, s45, 0
	s_lshl_b32 s4, s52, 10
	s_add_i32 s27, s4, 0
	s_waitcnt vmcnt(32)
	v_mov_b32_e32 v5, 0
	v_lshlrev_b32_e32 v4, 3, v194
	s_mul_i32 s4, s52, 0x3d00
	v_lshl_add_u64 v[2:3], s[44:45], 0, v[4:5]
	v_add_u32_e32 v9, s27, v4
	v_mbcnt_lo_u32_b32 v4, -1, 0
	s_add_i32 s28, s27, s4
	v_lshlrev_b32_e32 v1, 2, v194
	s_mov_b64 s[6:7], 0x98a98000
	v_mbcnt_hi_u32_b32 v12, -1, v4
	v_mov_b32_e32 v4, -1
	v_cmp_eq_u32_e64 s[4:5], 0, v194
	v_add_u32_e32 v8, s28, v1
	v_lshl_add_u64 v[2:3], v[2:3], 0, s[6:7]
	v_or_b32_e32 v10, 64, v194
	s_add_i32 s29, 0, 0x23fc0
	s_movk_i32 s30, 0xff
	v_lshlrev_b32_e32 v11, 1, v194
	s_movk_i32 s31, 0x7ff
	s_movk_i32 s34, 0x17ff
	s_brev_b32 s35, 1
	s_movk_i32 s36, 0x1ff
	s_movk_i32 s37, 0x2ff
	s_movk_i32 s38, 0x4ff
	s_movk_i32 s39, 0x5ff
	s_movk_i32 s40, 0x6ff
	s_movk_i32 s41, 0x8ff
	s_movk_i32 s42, 0x9ff
	s_movk_i32 s43, 0xaff
	s_movk_i32 s49, 0xcff
	s_movk_i32 s53, 0xdff
	s_movk_i32 s54, 0xeff
	s_movk_i32 s55, 0xfff
	s_movk_i32 s56, 0x10ff
	s_movk_i32 s57, 0x11ff
	s_movk_i32 s58, 0x12ff
	s_movk_i32 s59, 0x14ff
	s_movk_i32 s60, 0x15ff
	s_movk_i32 s61, 0x16ff
	s_movk_i32 s62, 0x100
	s_movk_i32 s63, 0x4000
	s_movk_i32 s64, 0x3ff
	s_movk_i32 s65, 0xbff
	s_movk_i32 s67, 0x13ff
	v_mov_b32_e32 v13, 0x100
	v_mov_b32_e32 v5, v4
	s_branch .LBB0_522
